# six staging waves per CU (no static LDS), stream block behind the 15th PV MFMA, layer-1 items only
# baseline (speedup 1.0000x reference)
; __device__ __forceinline__ void convert_moe_items(const Ctx& a, int layer, LAS unsigned char* lds, int it0, int it1, int widx, int nw, int wave, int lane) {
;     ...
;     auto decode = [&](int it) { CvtItem d; const int e = it / PER_E; int r = it % PER_E; const size_t eo = ((size_t)layer * NE + e) * (size_t)DM * FE;
;         if (r < I_G)          { d.src = wg + eo; d.dst = WGU; d.N = FE; d.K = DM; d.row_off = e * 2048; d.ilv = 1; }
;         else if (r < 2 * I_G) { r -= I_G; d.src = wu + eo; d.dst = WGU; d.N = FE; d.K = DM; d.row_off = e * 2048 + 128; d.ilv = 1; }
;         else                  { r -= 2 * I_G; d.src = wd + eo; d.dst = WD; d.N = DM; d.K = FE; d.row_off = e * 2048; d.ilv = 0; }
;         const int nblk = d.N / 32; d.k0 = 64 * (r / nblk); d.n0 = 32 * (r % nblk); return d; };
.Lcs_dec_h0:
	s_cmp_lt_u32 s66, 0xa800
	s_cbranch_scc1 .Lcs_id_h0
	s_bitcmp1_b32 s66, 16
	s_cbranch_scc1 .Lcs_id_h0
	s_add_i32 s66, s66, 0x11800
.Lcs_id_h0:
	s_and_b32 s3, s66, 0xffff
	s_lshr_b32 s91, s66, 16
	s_mul_i32 s78, s3, 0xaaab
	s_lshr_b32 s78, s78, 27
	s_mul_i32 s79, s78, 0xc00
	s_sub_i32 s79, s3, s79
	s_addk_i32 s66, 0x600
	s_xor_b32 s80, s91, 1
	s_lshl_b32 s80, s80, 4
	s_add_i32 s80, s80, s78
	s_lshl_b32 s80, s80, 23
	s_lshl_b32 s91, s91, 27
	s_lshl_b32 s81, s78, 11
	s_cmpk_gt_u32 s79, 0x7ff
	s_cbranch_scc1 .Lcs_down_h0
	s_mov_b64 s[98:99], s[68:69]
	s_cmpk_gt_u32 s79, 0x3ff
	s_cbranch_scc0 .Lcs_gate_h0
	s_mov_b64 s[98:99], s[70:71]
	s_addk_i32 s81, 0x80
	s_addk_i32 s79, 0xfc00
